# v35: SGU unit epilogue: the 8 per-row biases loaded up front, per-row vmcnt(0) (which also drained the previous row's store) replaced by counted waits
# baseline (speedup 1.0000x reference)
; #define GAS __attribute__((address_space(1)))
; #define LAS __attribute__((address_space(3)))
; __device__ __forceinline__ unsigned pk2(float lo, float hi) { return pg8::cvt_pk_bf16(lo, hi); }
; __device__ __forceinline__ void sgu_unit(Frame& F, int unit) {
;     ...
;     __syncthreads();
; #pragma unroll
;     for (int i = 0; i < 8; ++i) *(LAS v4u*)(L + (rs_ + 16 * i) * 512 + q_ * 16) = *(const GAS v4u*)(F.PROJ + (size_t)(r0 + rs_ + 16 * i) * PNP + PGV + c0 + 8 * q_);
;     { const f32x4 q = *(const GAS f32x4*)(F.RS + r0 + 4 * q_);
; #pragma unroll
;       for (int i = 0; i < 8; ++i) { const int t_ = rs_ + 16 * i; const f32x4 wv = *(const GAS f32x4*)(F.sgw + ((size_t)(g * GMC + t_)) * GMC + 4 * q_);
;           const int sb = 4 * q_; v2u o;
;           o.x = pk2(sb + 0 <= t_ ? wv.x * q.x : 0.f, sb + 1 <= t_ ? wv.y * q.y : 0.f); o.y = pk2(sb + 2 <= t_ ? wv.z * q.z : 0.f, sb + 3 <= t_ ? wv.w * q.w : 0.f);
;           *(LAS v2u*)(L + SG_WOFF + t_ * SG_STR + 8 * q_) = o; } }
.LBB0_1330:
	s_and_b32 s74, s33, 0xffffff80
	s_and_b32 s83, s82, 7
	v_or_b32_e32 v128, s74, v1
	v_mad_i64_i32 v[2:3], s[0:1], v128, s77, v[108:109]
	s_lshl_b32 s84, s83, 9
	s_mov_b32 s85, s73
	v_lshl_add_u64 v[2:3], v[2:3], 0, s[84:85]
	v_lshl_add_u64 v[2:3], v[2:3], 0, v[110:111]
	v_add_co_u32_e64 v4, s[0:1], s78, v2
	s_nop 1
	v_addc_co_u32_e64 v5, s[0:1], 0, v3, s[0:1]
	s_barrier
	global_load_dwordx4 v[28:31], v[4:5], off offset:2048
	v_or_b32_e32 v126, 16, v128
	v_or_b32_e32 v124, 32, v128
	v_or_b32_e32 v122, 48, v128
	v_or_b32_e32 v120, 64, v128
	v_or_b32_e32 v118, 0x50, v128
	v_or_b32_e32 v116, 0x60, v128
	v_or_b32_e32 v114, 0x70, v128
	s_ashr_i32 s75, s74, 31
	v_ashrrev_i32_e32 v129, 31, v128
	s_lshl_b32 s72, s83, 8
	v_ashrrev_i32_e32 v127, 31, v126
	v_ashrrev_i32_e32 v125, 31, v124
	v_ashrrev_i32_e32 v123, 31, v122
	v_ashrrev_i32_e32 v121, 31, v120
	v_ashrrev_i32_e32 v119, 31, v118
	v_ashrrev_i32_e32 v117, 31, v116
	v_ashrrev_i32_e32 v115, 31, v114
	v_readlane_b32 s89, v248, 15
	s_add_i32 s82, s82, s89
	s_add_i32 s33, s33, s76
	v_mad_i64_i32 v[4:5], s[0:1], v126, s77, v[108:109]
	v_lshl_add_u64 v[4:5], v[4:5], 0, s[84:85]
	v_lshl_add_u64 v[4:5], v[4:5], 0, v[110:111]
	v_add_co_u32_e64 v26, s[0:1], s78, v4
	s_nop 1
	v_addc_co_u32_e64 v27, s[0:1], 0, v5, s[0:1]
	global_load_dwordx4 v[32:35], v[26:27], off offset:2048
	v_mad_i64_i32 v[6:7], s[0:1], v124, s77, v[108:109]
	v_lshl_add_u64 v[6:7], v[6:7], 0, s[84:85]
	v_lshl_add_u64 v[6:7], v[6:7], 0, v[110:111]
	v_add_co_u32_e64 v26, s[0:1], s78, v6
	s_nop 1
	v_addc_co_u32_e64 v27, s[0:1], 0, v7, s[0:1]
	global_load_dwordx4 v[36:39], v[26:27], off offset:2048
	v_mad_i64_i32 v[8:9], s[0:1], v122, s77, v[108:109]
	v_lshl_add_u64 v[8:9], v[8:9], 0, s[84:85]
	v_lshl_add_u64 v[8:9], v[8:9], 0, v[110:111]
	v_add_co_u32_e64 v26, s[0:1], s78, v8
	s_nop 1
	v_addc_co_u32_e64 v27, s[0:1], 0, v9, s[0:1]
	global_load_dwordx4 v[40:43], v[26:27], off offset:2048
	v_mad_i64_i32 v[10:11], s[0:1], v120, s77, v[108:109]
	v_lshl_add_u64 v[10:11], v[10:11], 0, s[84:85]
	v_lshl_add_u64 v[10:11], v[10:11], 0, v[110:111]
	v_add_co_u32_e64 v26, s[0:1], s78, v10
	s_nop 1
	v_addc_co_u32_e64 v27, s[0:1], 0, v11, s[0:1]
	global_load_dwordx4 v[44:47], v[26:27], off offset:2048
	v_mad_i64_i32 v[12:13], s[0:1], v118, s77, v[108:109]
	v_lshl_add_u64 v[12:13], v[12:13], 0, s[84:85]
	v_lshl_add_u64 v[12:13], v[12:13], 0, v[110:111]
	v_add_co_u32_e64 v26, s[0:1], s78, v12
	s_nop 1
	v_addc_co_u32_e64 v27, s[0:1], 0, v13, s[0:1]
	global_load_dwordx4 v[48:51], v[26:27], off offset:2048
	v_mad_i64_i32 v[14:15], s[0:1], v116, s77, v[108:109]
	v_lshl_add_u64 v[14:15], v[14:15], 0, s[84:85]
	v_lshl_add_u64 v[14:15], v[14:15], 0, v[110:111]
	v_add_co_u32_e64 v26, s[0:1], s78, v14
	s_nop 1
	v_addc_co_u32_e64 v27, s[0:1], 0, v15, s[0:1]
	global_load_dwordx4 v[52:55], v[26:27], off offset:2048
	v_mad_i64_i32 v[16:17], s[0:1], v114, s77, v[108:109]
	v_lshl_add_u64 v[16:17], v[16:17], 0, s[84:85]
	v_lshl_add_u64 v[16:17], v[16:17], 0, v[110:111]
	v_add_co_u32_e64 v26, s[0:1], s78, v16
	s_nop 1
	v_addc_co_u32_e64 v27, s[0:1], 0, v17, s[0:1]
	global_load_dwordx4 v[56:59], v[26:27], off offset:2048
	s_lshl_b32 s0, s83, 7
	v_or_b32_e32 v113, s0, v1
	v_lshl_add_u64 v[18:19], s[74:75], 2, v[102:103]
	global_load_dwordx4 v[18:21], v[18:19], off
	v_lshlrev_b32_e32 v100, 9, v113
	v_lshl_add_u64 v[22:23], v[104:105], 0, v[100:101]
	global_load_dwordx4 v[60:63], v[22:23], off
	v_or_b32_e32 v22, s0, v130
	v_lshlrev_b32_e32 v100, 9, v22
	v_lshl_add_u64 v[22:23], v[104:105], 0, v[100:101]
	global_load_dwordx4 v[64:67], v[22:23], off
	v_or_b32_e32 v22, s0, v131
	v_lshlrev_b32_e32 v100, 9, v22
	v_lshl_add_u64 v[22:23], v[104:105], 0, v[100:101]
	global_load_dwordx4 v[68:71], v[22:23], off
	v_or_b32_e32 v22, s0, v132
	v_lshlrev_b32_e32 v100, 9, v22
	v_lshl_add_u64 v[22:23], v[104:105], 0, v[100:101]
	global_load_dwordx4 v[72:75], v[22:23], off
	v_or_b32_e32 v22, s0, v133
	v_lshlrev_b32_e32 v100, 9, v22
	v_lshl_add_u64 v[22:23], v[104:105], 0, v[100:101]
	global_load_dwordx4 v[76:79], v[22:23], off
	v_or_b32_e32 v22, s0, v134
	v_lshlrev_b32_e32 v100, 9, v22
	v_lshl_add_u64 v[22:23], v[104:105], 0, v[100:101]
	global_load_dwordx4 v[80:83], v[22:23], off
	v_or_b32_e32 v22, s0, v135
	v_lshlrev_b32_e32 v100, 9, v22
	v_lshl_add_u64 v[22:23], v[104:105], 0, v[100:101]
	global_load_dwordx4 v[84:87], v[22:23], off
	v_or_b32_e32 v22, s0, v136
	v_lshlrev_b32_e32 v100, 9, v22
	v_lshl_add_u64 v[22:23], v[104:105], 0, v[100:101]
	global_load_dwordx4 v[88:91], v[22:23], off
	s_waitcnt vmcnt(16)
	ds_write_b128 v139, v[28:31]
	s_waitcnt vmcnt(15)
	ds_write_b128 v140, v[32:35]
	s_waitcnt vmcnt(14)
	ds_write_b128 v141, v[36:39]
	s_waitcnt vmcnt(13)
	ds_write_b128 v142, v[40:43]
	s_waitcnt vmcnt(12)
	ds_write_b128 v143, v[44:47]
	s_waitcnt vmcnt(11)
	ds_write_b128 v144, v[48:51]
	s_waitcnt vmcnt(10)
	ds_write_b128 v145, v[52:55]
	s_waitcnt vmcnt(9)
	ds_write_b128 v146, v[56:59]
	s_waitcnt vmcnt(7)
	v_mul_f32_e32 v22, v18, v60
	v_mul_f32_e32 v23, v19, v61
	v_cndmask_b32_e64 v22, v22, 0, s[70:71]
	v_cndmask_b32_e64 v23, 0, v23, s[4:5]
	v_cvt_pk_bf16_f32 v22, v22, v23
	v_mul_f32_e32 v23, v20, v62
	v_cndmask_b32_e64 v23, v23, 0, s[6:7]
	v_mul_f32_e32 v24, v21, v63
	v_cndmask_b32_e64 v24, v24, 0, s[86:87]
	v_cvt_pk_bf16_f32 v23, v23, v24
	ds_write_b64 v147, v[22:23]
	s_waitcnt vmcnt(6)
	v_mul_f32_e32 v22, v18, v64
	v_mul_f32_e32 v23, v19, v65
	v_cndmask_b32_e64 v22, v22, 0, s[90:91]
	v_cndmask_b32_e64 v23, 0, v23, s[92:93]
	v_cvt_pk_bf16_f32 v22, v22, v23
	v_mul_f32_e32 v23, v20, v66
	v_cndmask_b32_e64 v23, v23, 0, s[94:95]
	v_mul_f32_e32 v24, v21, v67
	v_cndmask_b32_e64 v24, v24, 0, s[96:97]
	v_cvt_pk_bf16_f32 v23, v23, v24
	ds_write_b64 v147, v[22:23] offset:4352
	s_waitcnt vmcnt(5)
; #define GAS __attribute__((address_space(1)))
; #define LAS __attribute__((address_space(3)))
; __device__ __forceinline__ unsigned pk2(float lo, float hi) { return pg8::cvt_pk_bf16(lo, hi); }
; __device__ __forceinline__ void sgu_unit(Frame& F, int unit) {
;     ...
;       for (int i = 0; i < 8; ++i) { const int t_ = rs_ + 16 * i; const f32x4 wv = *(const GAS f32x4*)(F.sgw + ((size_t)(g * GMC + t_)) * GMC + 4 * q_);
;           const int sb = 4 * q_; v2u o;
;           o.x = pk2(sb + 0 <= t_ ? wv.x * q.x : 0.f, sb + 1 <= t_ ? wv.y * q.y : 0.f); o.y = pk2(sb + 2 <= t_ ? wv.z * q.z : 0.f, sb + 3 <= t_ ? wv.w * q.w : 0.f);
;           *(LAS v2u*)(L + SG_WOFF + t_ * SG_STR + 8 * q_) = o; } }
;     __syncthreads();
;     v4u uu[8];
; #pragma unroll
;     for (int i = 0; i < 8; ++i) uu[i] = *(const GAS v4u*)(F.PROJ + (size_t)(r0 + rs_ + 16 * i) * PNP + PGU + c0 + 8 * q_);
;     f32x16 acc[4];
; #pragma unroll
;     for (int tb = 0; tb < 4; ++tb)
; #pragma unroll
;         for (int r = 0; r < 16; ++r) acc[tb][r] = 0.f;
;     const LAS unsigned char* xb = L + hi * 8 * 512 + 2 * (32 * w + l31);
;     const LAS unsigned char* wa = L + SG_WOFF + l31 * SG_STR + hi * 16;
; #pragma unroll
;     for (int ks = 0; ks < 8; ++ks) {
;         v4u xw;
; #pragma unroll
;         for (int j = 0; j < 4; ++j) { const unsigned lo = *(const LAS unsigned short*)(xb + (16 * ks + 2 * j) * 512), hh = *(const LAS unsigned short*)(xb + (16 * ks + 2 * j + 1) * 512); xw[j] = lo | (hh << 16); }
;         const bf16x8 xf = __builtin_bit_cast(bf16x8, xw);
; #pragma unroll
;         for (int tb = 0; tb < 4; ++tb) if (ks < 2 * (tb + 1)) { const bf16x8 wf = *(const LAS bf16x8*)(wa + tb * 32 * SG_STR + ks * 32); acc[tb] = __builtin_amdgcn_mfma_f32_32x32x16_bf16(wf, xf, acc[tb], 0, 0, 0); } }
	v_mul_f32_e32 v22, v18, v68
	v_mul_f32_e32 v23, v19, v69
	v_cndmask_b32_e64 v22, v22, 0, vcc
	v_cndmask_b32_e64 v23, 0, v23, s[2:3]
	v_cvt_pk_bf16_f32 v22, v22, v23
	v_mul_f32_e32 v23, v20, v70
	v_cndmask_b32_e64 v23, v23, 0, s[20:21]
	v_mul_f32_e32 v24, v21, v71
	v_cndmask_b32_e64 v24, v24, 0, s[22:23]
	v_cvt_pk_bf16_f32 v23, v23, v24
	ds_write_b64 v147, v[22:23] offset:8704
	s_waitcnt vmcnt(4)
	v_mul_f32_e32 v22, v18, v72
	v_mul_f32_e32 v23, v19, v73
	v_cndmask_b32_e64 v22, v22, 0, s[24:25]
	v_cndmask_b32_e64 v23, 0, v23, s[26:27]
	v_cvt_pk_bf16_f32 v22, v22, v23
	v_mul_f32_e32 v23, v20, v74
	v_cndmask_b32_e64 v23, v23, 0, s[28:29]
	v_mul_f32_e32 v24, v21, v75
	v_cndmask_b32_e64 v24, v24, 0, s[30:31]
	v_cvt_pk_bf16_f32 v23, v23, v24
	ds_write_b64 v147, v[22:23] offset:13056
	s_waitcnt vmcnt(3)
	v_mul_f32_e32 v22, v18, v76
	v_mul_f32_e32 v23, v19, v77
	v_cndmask_b32_e64 v22, v22, 0, s[34:35]
	v_cndmask_b32_e64 v23, 0, v23, s[36:37]
	v_cvt_pk_bf16_f32 v22, v22, v23
	v_mul_f32_e32 v23, v20, v78
	v_cndmask_b32_e64 v23, v23, 0, s[38:39]
	v_mul_f32_e32 v24, v21, v79
	v_cndmask_b32_e64 v24, v24, 0, s[40:41]
	v_cvt_pk_bf16_f32 v23, v23, v24
	ds_write_b64 v147, v[22:23] offset:17408
	s_waitcnt vmcnt(2)
	v_mul_f32_e32 v22, v18, v80
	v_mul_f32_e32 v23, v19, v81
	v_cndmask_b32_e64 v22, v22, 0, s[42:43]
	v_cndmask_b32_e64 v23, 0, v23, s[66:67]
	v_cvt_pk_bf16_f32 v22, v22, v23
	v_mul_f32_e32 v23, v20, v82
	v_cndmask_b32_e64 v23, v23, 0, s[46:47]
	v_mul_f32_e32 v24, v21, v83
	v_cndmask_b32_e64 v24, v24, 0, s[48:49]
	v_cvt_pk_bf16_f32 v23, v23, v24
	ds_write_b64 v147, v[22:23] offset:21760
	s_waitcnt vmcnt(1)
	v_mul_f32_e32 v22, v18, v84
	v_mul_f32_e32 v23, v19, v85
	v_cndmask_b32_e64 v22, v22, 0, s[50:51]
	v_cndmask_b32_e64 v23, 0, v23, s[52:53]
	v_cvt_pk_bf16_f32 v22, v22, v23
	v_mul_f32_e32 v23, v20, v86
	v_cndmask_b32_e64 v23, v23, 0, s[54:55]
	v_mul_f32_e32 v24, v21, v87
	v_cndmask_b32_e64 v24, v24, 0, s[56:57]
	v_cvt_pk_bf16_f32 v23, v23, v24
	ds_write_b64 v147, v[22:23] offset:26112
	s_waitcnt vmcnt(0)
	v_add_co_u32_e64 v2, s[0:1], s79, v2
	v_mul_f32_e32 v18, v18, v88
	v_mul_f32_e32 v19, v19, v89
	v_cndmask_b32_e64 v18, v18, 0, s[58:59]
	v_cndmask_b32_e64 v19, 0, v19, s[60:61]
	v_cvt_pk_bf16_f32 v18, v18, v19
	v_mul_f32_e32 v19, v20, v90
	v_cndmask_b32_e64 v19, v19, 0, s[62:63]
	v_mul_f32_e32 v20, v21, v91
	v_addc_co_u32_e64 v3, s[0:1], 0, v3, s[0:1]
	v_cndmask_b32_e64 v20, v20, 0, s[64:65]
	v_cvt_pk_bf16_f32 v19, v19, v20
	ds_write_b64 v147, v[18:19] offset:30464
	s_waitcnt lgkmcnt(0)
	s_barrier
	global_load_dwordx4 v[94:97], v[2:3], off offset:2048
	v_add_co_u32_e64 v2, s[0:1], s79, v4
	s_nop 1
	v_addc_co_u32_e64 v3, s[0:1], 0, v5, s[0:1]
	global_load_dwordx4 v[90:93], v[2:3], off offset:2048
	v_add_co_u32_e64 v2, s[0:1], s79, v6
	s_nop 1
	v_addc_co_u32_e64 v3, s[0:1], 0, v7, s[0:1]
	global_load_dwordx4 v[86:89], v[2:3], off offset:2048
	v_add_co_u32_e64 v2, s[0:1], s79, v8
	s_nop 1
	v_addc_co_u32_e64 v3, s[0:1], 0, v9, s[0:1]
	global_load_dwordx4 v[82:85], v[2:3], off offset:2048
	v_add_co_u32_e64 v2, s[0:1], s79, v10
	s_nop 1
	v_addc_co_u32_e64 v3, s[0:1], 0, v11, s[0:1]
	global_load_dwordx4 v[78:81], v[2:3], off offset:2048
	v_add_co_u32_e64 v2, s[0:1], s79, v12
	s_nop 1
	v_addc_co_u32_e64 v3, s[0:1], 0, v13, s[0:1]
	global_load_dwordx4 v[74:77], v[2:3], off offset:2048
	v_add_co_u32_e64 v2, s[0:1], s79, v14
	s_nop 1
	v_addc_co_u32_e64 v3, s[0:1], 0, v15, s[0:1]
	global_load_dwordx4 v[70:73], v[2:3], off offset:2048
	v_add_co_u32_e64 v2, s[0:1], s79, v16
	s_nop 1
	v_addc_co_u32_e64 v3, s[0:1], 0, v17, s[0:1]
	global_load_dwordx4 v[66:69], v[2:3], off offset:2048
	ds_read_u16 v2, v137
	ds_read_u16 v3, v137 offset:512
	s_lshl_b32 s0, s83, 10
	s_mov_b32 s1, s73
	s_cmpk_gt_i32 s82, 0x1ff
	s_waitcnt lgkmcnt(0)
	v_lshl_or_b32 v2, v3, 16, v2
	ds_read_u16 v3, v137 offset:1024
	ds_read_u16 v4, v137 offset:1536
	s_waitcnt lgkmcnt(0)
	v_lshl_or_b32 v3, v4, 16, v3
	ds_read_u16 v4, v137 offset:2048
	ds_read_u16 v5, v137 offset:2560
	s_waitcnt lgkmcnt(0)
	v_lshl_or_b32 v4, v5, 16, v4
	ds_read_u16 v5, v137 offset:3072
	ds_read_u16 v6, v137 offset:3584
	s_waitcnt lgkmcnt(0)
	v_lshl_or_b32 v5, v6, 16, v5
	ds_read_b128 v[6:9], v148
	ds_read_b128 v[150:153], v148 offset:32
	s_waitcnt lgkmcnt(1)
	v_mfma_f32_32x32x16_bf16 v[50:65], v[6:9], v[2:5], 0
	ds_read_b128 v[6:9], v148 offset:8704
	s_waitcnt lgkmcnt(0)
	v_mfma_f32_32x32x16_bf16 v[34:49], v[6:9], v[2:5], 0
	ds_read_b128 v[6:9], v148 offset:17408
	s_waitcnt lgkmcnt(0)
	v_mfma_f32_32x32x16_bf16 v[18:33], v[6:9], v[2:5], 0
	ds_read_b128 v[6:9], v148 offset:26112
	ds_read_u16 v100, v137 offset:8192
	ds_read_u16 v154, v137 offset:8704
	s_waitcnt lgkmcnt(0)
	v_lshl_or_b32 v154, v154, 16, v100
	ds_read_u16 v100, v137 offset:9216
	ds_read_u16 v155, v137 offset:9728
	v_mfma_f32_32x32x16_bf16 v[2:17], v[6:9], v[2:5], 0
	s_waitcnt lgkmcnt(0)
	v_lshl_or_b32 v155, v155, 16, v100
	ds_read_u16 v100, v137 offset:10240
	ds_read_u16 v156, v137 offset:10752
	s_waitcnt lgkmcnt(0)
	v_lshl_or_b32 v156, v156, 16, v100
	ds_read_u16 v100, v137 offset:11264
	ds_read_u16 v157, v137 offset:11776
	s_waitcnt lgkmcnt(0)
	v_lshl_or_b32 v157, v157, 16, v100
	s_nop 1
	v_mfma_f32_32x32x16_bf16 v[50:65], v[150:153], v[154:157], v[50:65]
	ds_read_b128 v[150:153], v148 offset:8736
	s_waitcnt lgkmcnt(0)
	v_mfma_f32_32x32x16_bf16 v[34:49], v[150:153], v[154:157], v[34:49]
	ds_read_b128 v[150:153], v148 offset:17440
	s_waitcnt lgkmcnt(0)
	v_mfma_f32_32x32x16_bf16 v[18:33], v[150:153], v[154:157], v[18:33]
	ds_read_b128 v[150:153], v148 offset:26144
	s_waitcnt lgkmcnt(0)
; #define LAS __attribute__((address_space(3)))
; #define LDS_WAIT() asm volatile("s_waitcnt lgkmcnt(0)" ::: "memory")
; __device__ __forceinline__ void sgu_unit(Frame& F, int unit) {
;     ...
; #pragma unroll
;     for (int ks = 0; ks < 8; ++ks) {
;         v4u xw;
; #pragma unroll
;         for (int j = 0; j < 4; ++j) { const unsigned lo = *(const LAS unsigned short*)(xb + (16 * ks + 2 * j) * 512), hh = *(const LAS unsigned short*)(xb + (16 * ks + 2 * j + 1) * 512); xw[j] = lo | (hh << 16); }
;         const bf16x8 xf = __builtin_bit_cast(bf16x8, xw);
; #pragma unroll
;         for (int tb = 0; tb < 4; ++tb) if (ks < 2 * (tb + 1)) { const bf16x8 wf = *(const LAS bf16x8*)(wa + tb * 32 * SG_STR + ks * 32); acc[tb] = __builtin_amdgcn_mfma_f32_32x32x16_bf16(wf, xf, acc[tb], 0, 0, 0); } }
;     LDS_WAIT(); __builtin_amdgcn_s_barrier(); asm volatile("" ::: "memory");
	v_mfma_f32_32x32x16_bf16 v[2:17], v[150:153], v[154:157], v[2:17]
	ds_read_u16 v100, v137 offset:16384
	ds_read_u16 v150, v137 offset:16896
	s_waitcnt lgkmcnt(0)
	v_lshl_or_b32 v150, v150, 16, v100
	ds_read_u16 v100, v137 offset:17408
	ds_read_u16 v151, v137 offset:17920
	s_waitcnt lgkmcnt(0)
	v_lshl_or_b32 v151, v151, 16, v100
	ds_read_u16 v100, v137 offset:18432
	ds_read_u16 v152, v137 offset:18944
	s_waitcnt lgkmcnt(0)
	v_lshl_or_b32 v152, v152, 16, v100
	ds_read_u16 v100, v137 offset:19456
	ds_read_u16 v153, v137 offset:19968
	ds_read_b128 v[154:157], v148 offset:8768
	s_waitcnt lgkmcnt(1)
	v_lshl_or_b32 v153, v153, 16, v100
	s_waitcnt lgkmcnt(0)
	s_nop 0
	v_mfma_f32_32x32x16_bf16 v[34:49], v[154:157], v[150:153], v[34:49]
	ds_read_b128 v[154:157], v148 offset:17472
	s_waitcnt lgkmcnt(0)
	v_mfma_f32_32x32x16_bf16 v[18:33], v[154:157], v[150:153], v[18:33]
	ds_read_b128 v[154:157], v148 offset:26176
	s_waitcnt lgkmcnt(0)
	v_mfma_f32_32x32x16_bf16 v[2:17], v[154:157], v[150:153], v[2:17]
	ds_read_u16 v100, v137 offset:24576
	ds_read_u16 v150, v137 offset:25088
	s_waitcnt lgkmcnt(0)
	v_lshl_or_b32 v150, v150, 16, v100
	ds_read_u16 v100, v137 offset:25600
	ds_read_u16 v151, v137 offset:26112
	s_waitcnt lgkmcnt(0)
	v_lshl_or_b32 v151, v151, 16, v100
	ds_read_u16 v100, v137 offset:26624
	ds_read_u16 v152, v137 offset:27136
	s_waitcnt lgkmcnt(0)
	v_lshl_or_b32 v152, v152, 16, v100
	ds_read_u16 v100, v137 offset:27648
	ds_read_u16 v153, v137 offset:28160
	ds_read_b128 v[154:157], v148 offset:8800
	s_waitcnt lgkmcnt(1)
	v_lshl_or_b32 v153, v153, 16, v100
	s_waitcnt lgkmcnt(0)
	s_nop 0
	v_mfma_f32_32x32x16_bf16 v[34:49], v[154:157], v[150:153], v[34:49]
	ds_read_b128 v[154:157], v148 offset:17504
	s_waitcnt lgkmcnt(0)
	v_mfma_f32_32x32x16_bf16 v[18:33], v[154:157], v[150:153], v[18:33]
	ds_read_b128 v[154:157], v148 offset:26208
	s_waitcnt lgkmcnt(0)
	v_mfma_f32_32x32x16_bf16 v[2:17], v[154:157], v[150:153], v[2:17]
	ds_read_u16 v100, v137 offset:32768
	ds_read_u16 v150, v137 offset:33280
	s_waitcnt lgkmcnt(0)
	v_lshl_or_b32 v150, v150, 16, v100
	ds_read_u16 v100, v137 offset:33792
	ds_read_u16 v151, v137 offset:34304
	s_waitcnt lgkmcnt(0)
	v_lshl_or_b32 v151, v151, 16, v100
	ds_read_u16 v100, v137 offset:34816
	ds_read_u16 v152, v137 offset:35328
	s_waitcnt lgkmcnt(0)
	v_lshl_or_b32 v152, v152, 16, v100
	ds_read_u16 v100, v137 offset:35840
	ds_read_u16 v153, v137 offset:36352
	ds_read_b128 v[154:157], v148 offset:17536
	s_waitcnt lgkmcnt(1)
	v_lshl_or_b32 v153, v153, 16, v100
	s_waitcnt lgkmcnt(0)
	s_nop 0
	v_mfma_f32_32x32x16_bf16 v[18:33], v[154:157], v[150:153], v[18:33]
	ds_read_b128 v[154:157], v148 offset:26240
	s_waitcnt lgkmcnt(0)
	v_mfma_f32_32x32x16_bf16 v[2:17], v[154:157], v[150:153], v[2:17]
	ds_read_u16 v100, v137 offset:40960
	ds_read_u16 v150, v137 offset:41472
	s_waitcnt lgkmcnt(0)
	v_lshl_or_b32 v150, v150, 16, v100
	ds_read_u16 v100, v137 offset:41984
	ds_read_u16 v151, v137 offset:42496
	s_waitcnt lgkmcnt(0)
	v_lshl_or_b32 v151, v151, 16, v100
	ds_read_u16 v100, v137 offset:43008
	ds_read_u16 v152, v137 offset:43520
	s_waitcnt lgkmcnt(0)
	v_lshl_or_b32 v152, v152, 16, v100
	ds_read_u16 v100, v137 offset:44032
	ds_read_u16 v153, v137 offset:44544
	ds_read_b128 v[154:157], v148 offset:17568
	s_waitcnt lgkmcnt(1)
	v_lshl_or_b32 v153, v153, 16, v100
	s_waitcnt lgkmcnt(0)
	s_nop 0
	v_mfma_f32_32x32x16_bf16 v[18:33], v[154:157], v[150:153], v[18:33]
	ds_read_b128 v[154:157], v148 offset:26272
	s_waitcnt lgkmcnt(0)
	v_mfma_f32_32x32x16_bf16 v[2:17], v[154:157], v[150:153], v[2:17]
	ds_read_u16 v100, v137 offset:49152
	ds_read_u16 v150, v137 offset:49664
	s_waitcnt lgkmcnt(0)
	v_lshl_or_b32 v150, v150, 16, v100
	ds_read_u16 v100, v137 offset:50176
	ds_read_u16 v151, v137 offset:50688
	s_waitcnt lgkmcnt(0)
	v_lshl_or_b32 v151, v151, 16, v100
	ds_read_u16 v100, v137 offset:51200
	ds_read_u16 v152, v137 offset:51712
	s_waitcnt lgkmcnt(0)
	v_lshl_or_b32 v152, v152, 16, v100
	ds_read_u16 v100, v137 offset:52224
	ds_read_u16 v153, v137 offset:52736
	ds_read_b128 v[154:157], v148 offset:26304
	s_waitcnt lgkmcnt(1)
	v_lshl_or_b32 v153, v153, 16, v100
	s_waitcnt lgkmcnt(0)
	s_nop 0
	v_mfma_f32_32x32x16_bf16 v[2:17], v[154:157], v[150:153], v[2:17]
	ds_read_u16 v100, v137 offset:57344
	ds_read_u16 v150, v137 offset:57856
	s_waitcnt lgkmcnt(0)
	v_lshl_or_b32 v150, v150, 16, v100
	ds_read_u16 v100, v137 offset:58368
	ds_read_u16 v151, v137 offset:58880
	s_waitcnt lgkmcnt(0)
	v_lshl_or_b32 v151, v151, 16, v100
	ds_read_u16 v100, v137 offset:59392
	ds_read_u16 v152, v137 offset:59904
	s_waitcnt lgkmcnt(0)
	v_lshl_or_b32 v152, v152, 16, v100
	ds_read_u16 v100, v137 offset:60416
	ds_read_u16 v153, v137 offset:60928
	ds_read_b128 v[154:157], v148 offset:26336
	s_waitcnt lgkmcnt(0)
	s_barrier
; #define GAS __attribute__((address_space(1)))
; #define LAS __attribute__((address_space(3)))
; #define LDS_WAIT() asm volatile("s_waitcnt lgkmcnt(0)" ::: "memory")
; __device__ __forceinline__ unsigned f2bf(float f) { unsigned u = __builtin_bit_cast(unsigned, f); return (u + 0x7fffu + ((u >> 16) & 1u)) >> 16; }
; __device__ __forceinline__ void sgu_unit(Frame& F, int unit) {
;     ...
;     LDS_WAIT(); __builtin_amdgcn_s_barrier(); asm volatile("" ::: "memory");
;     { const int cl = 32 * w + l31;
; #pragma unroll
;       for (int tb = 0; tb < 4; ++tb)
; #pragma unroll
;           for (int r = 0; r < 16; ++r) { const int t = 32 * tb + (r & 3) + 8 * (r >> 2) + 4 * hi; *(LAS unsigned short*)(L + t * 512 + 2 * cl) = (unsigned short)f2bf(acc[tb][r]); } }
;     const f32x4 g0 = *(const GAS f32x4*)(F.sgg + c0 + 8 * q_), g1 = *(const GAS f32x4*)(F.sgg + c0 + 8 * q_ + 4);
;     LDS_WAIT(); __builtin_amdgcn_s_barrier(); asm volatile("" ::: "memory");
	s_waitcnt lgkmcnt(1)
	v_lshl_or_b32 v153, v153, 16, v100
	v_bfe_u32 v100, v50, 16, 1
	v_add3_u32 v50, v50, v100, s80
	ds_write_b16_d16_hi v138, v50
	v_bfe_u32 v50, v51, 16, 1
	v_add3_u32 v50, v51, v50, s80
	ds_write_b16_d16_hi v138, v50 offset:512
	v_bfe_u32 v50, v52, 16, 1
	v_add3_u32 v50, v52, v50, s80
	ds_write_b16_d16_hi v138, v50 offset:1024
	v_bfe_u32 v50, v53, 16, 1
	v_add3_u32 v50, v53, v50, s80
	ds_write_b16_d16_hi v138, v50 offset:1536
	v_bfe_u32 v50, v54, 16, 1
	v_add3_u32 v50, v54, v50, s80
	ds_write_b16_d16_hi v138, v50 offset:4096
	v_bfe_u32 v50, v55, 16, 1
	v_add3_u32 v50, v55, v50, s80
	ds_write_b16_d16_hi v138, v50 offset:4608
	v_bfe_u32 v50, v56, 16, 1
	v_add3_u32 v50, v56, v50, s80
	ds_write_b16_d16_hi v138, v50 offset:5120
	v_bfe_u32 v50, v57, 16, 1
	v_add3_u32 v50, v57, v50, s80
	ds_write_b16_d16_hi v138, v50 offset:5632
	v_bfe_u32 v50, v58, 16, 1
	v_add3_u32 v50, v58, v50, s80
	ds_write_b16_d16_hi v138, v50 offset:8192
	v_bfe_u32 v50, v59, 16, 1
	v_add3_u32 v50, v59, v50, s80
	ds_write_b16_d16_hi v138, v50 offset:8704
	v_bfe_u32 v50, v60, 16, 1
	v_add3_u32 v50, v60, v50, s80
	ds_write_b16_d16_hi v138, v50 offset:9216
	v_bfe_u32 v50, v61, 16, 1
	v_add3_u32 v50, v61, v50, s80
	ds_write_b16_d16_hi v138, v50 offset:9728
	v_bfe_u32 v50, v62, 16, 1
	v_add3_u32 v50, v62, v50, s80
	ds_write_b16_d16_hi v138, v50 offset:12288
	v_bfe_u32 v50, v63, 16, 1
	v_add3_u32 v50, v63, v50, s80
	ds_write_b16_d16_hi v138, v50 offset:12800
	v_bfe_u32 v50, v64, 16, 1
	v_add3_u32 v50, v64, v50, s80
	ds_write_b16_d16_hi v138, v50 offset:13312
	v_bfe_u32 v50, v65, 16, 1
	v_add3_u32 v50, v65, v50, s80
	ds_write_b16_d16_hi v138, v50 offset:13824
	v_bfe_u32 v50, v34, 16, 1
	v_add3_u32 v34, v34, v50, s80
	ds_write_b16_d16_hi v138, v34 offset:16384
	v_bfe_u32 v34, v35, 16, 1
	v_add3_u32 v34, v35, v34, s80
	ds_write_b16_d16_hi v138, v34 offset:16896
	v_bfe_u32 v34, v36, 16, 1
	v_add3_u32 v34, v36, v34, s80
	ds_write_b16_d16_hi v138, v34 offset:17408
	v_bfe_u32 v34, v37, 16, 1
	v_add3_u32 v34, v37, v34, s80
	ds_write_b16_d16_hi v138, v34 offset:17920
	v_bfe_u32 v34, v38, 16, 1
	v_add3_u32 v34, v38, v34, s80
	ds_write_b16_d16_hi v138, v34 offset:20480
	v_bfe_u32 v34, v39, 16, 1
	v_add3_u32 v34, v39, v34, s80
	ds_write_b16_d16_hi v138, v34 offset:20992
	v_bfe_u32 v34, v40, 16, 1
	v_add3_u32 v34, v40, v34, s80
	ds_write_b16_d16_hi v138, v34 offset:21504
	v_bfe_u32 v34, v41, 16, 1
	v_add3_u32 v34, v41, v34, s80
	ds_write_b16_d16_hi v138, v34 offset:22016
	v_bfe_u32 v34, v42, 16, 1
	v_add3_u32 v34, v42, v34, s80
	ds_write_b16_d16_hi v138, v34 offset:24576
	v_bfe_u32 v34, v43, 16, 1
	v_add3_u32 v34, v43, v34, s80
	ds_write_b16_d16_hi v138, v34 offset:25088
	v_bfe_u32 v34, v44, 16, 1
	v_add3_u32 v34, v44, v34, s80
	ds_write_b16_d16_hi v138, v34 offset:25600
	v_bfe_u32 v34, v45, 16, 1
	v_add3_u32 v34, v45, v34, s80
	ds_write_b16_d16_hi v138, v34 offset:26112
	v_bfe_u32 v34, v46, 16, 1
	v_add3_u32 v34, v46, v34, s80
	ds_write_b16_d16_hi v138, v34 offset:28672
	v_bfe_u32 v34, v47, 16, 1
	v_add3_u32 v34, v47, v34, s80
	ds_write_b16_d16_hi v138, v34 offset:29184
	v_bfe_u32 v34, v48, 16, 1
	v_add3_u32 v34, v48, v34, s80
	ds_write_b16_d16_hi v138, v34 offset:29696
	v_bfe_u32 v34, v49, 16, 1
	v_add3_u32 v34, v49, v34, s80
	ds_write_b16_d16_hi v138, v34 offset:30208
	v_bfe_u32 v34, v18, 16, 1
	v_add3_u32 v18, v18, v34, s80
	ds_write_b16_d16_hi v138, v18 offset:32768
	v_bfe_u32 v18, v19, 16, 1
	v_add3_u32 v18, v19, v18, s80
	ds_write_b16_d16_hi v138, v18 offset:33280
	v_bfe_u32 v18, v20, 16, 1
	v_add3_u32 v18, v20, v18, s80
	ds_write_b16_d16_hi v138, v18 offset:33792
	v_bfe_u32 v18, v21, 16, 1
	v_add3_u32 v18, v21, v18, s80
	ds_write_b16_d16_hi v138, v18 offset:34304
	v_bfe_u32 v18, v22, 16, 1
	v_add3_u32 v18, v22, v18, s80
	ds_write_b16_d16_hi v138, v18 offset:36864
	v_bfe_u32 v18, v23, 16, 1
	v_add3_u32 v18, v23, v18, s80
	ds_write_b16_d16_hi v138, v18 offset:37376
	v_bfe_u32 v18, v24, 16, 1
	v_add3_u32 v18, v24, v18, s80
	ds_write_b16_d16_hi v138, v18 offset:37888
	v_bfe_u32 v18, v25, 16, 1
	v_add3_u32 v18, v25, v18, s80
	ds_write_b16_d16_hi v138, v18 offset:38400
	v_bfe_u32 v18, v26, 16, 1
	v_add3_u32 v18, v26, v18, s80
	ds_write_b16_d16_hi v138, v18 offset:40960
	v_bfe_u32 v18, v27, 16, 1
	v_add3_u32 v18, v27, v18, s80
	ds_write_b16_d16_hi v138, v18 offset:41472
	v_bfe_u32 v18, v28, 16, 1
	v_add3_u32 v18, v28, v18, s80
	ds_write_b16_d16_hi v138, v18 offset:41984
	v_bfe_u32 v18, v29, 16, 1
	v_add3_u32 v18, v29, v18, s80
	s_waitcnt lgkmcnt(14)
	v_mfma_f32_32x32x16_bf16 v[2:17], v[154:157], v[150:153], v[2:17]
	ds_write_b16_d16_hi v138, v18 offset:42496
	v_bfe_u32 v18, v30, 16, 1
	v_add3_u32 v18, v30, v18, s80
	ds_write_b16_d16_hi v138, v18 offset:45056
	v_bfe_u32 v18, v31, 16, 1
	v_add3_u32 v18, v31, v18, s80
	ds_write_b16_d16_hi v138, v18 offset:45568
	v_bfe_u32 v18, v32, 16, 1
	v_add3_u32 v18, v32, v18, s80
	ds_write_b16_d16_hi v138, v18 offset:46080
	v_bfe_u32 v18, v33, 16, 1
	v_add3_u32 v18, v33, v18, s80
	ds_write_b16_d16_hi v138, v18 offset:46592
	v_bfe_u32 v18, v2, 16, 1
	v_add3_u32 v2, v2, v18, s80
	ds_write_b16_d16_hi v138, v2 offset:49152
	v_bfe_u32 v2, v3, 16, 1
	v_add3_u32 v2, v3, v2, s80
	ds_write_b16_d16_hi v138, v2 offset:49664
	v_bfe_u32 v2, v4, 16, 1
	v_add3_u32 v2, v4, v2, s80
	ds_write_b16_d16_hi v138, v2 offset:50176
	v_bfe_u32 v2, v5, 16, 1
	v_add3_u32 v2, v5, v2, s80
	ds_write_b16_d16_hi v138, v2 offset:50688
	v_bfe_u32 v2, v6, 16, 1
	v_add3_u32 v2, v6, v2, s80
	ds_write_b16_d16_hi v138, v2 offset:53248
	v_bfe_u32 v2, v7, 16, 1
	v_add3_u32 v2, v7, v2, s80
	ds_write_b16_d16_hi v138, v2 offset:53760
	v_bfe_u32 v2, v8, 16, 1
	v_add3_u32 v2, v8, v2, s80
	ds_write_b16_d16_hi v138, v2 offset:54272
	v_bfe_u32 v2, v9, 16, 1
	v_add3_u32 v2, v9, v2, s80
	ds_write_b16_d16_hi v138, v2 offset:54784
	v_bfe_u32 v2, v10, 16, 1
	v_add3_u32 v2, v10, v2, s80
	ds_write_b16_d16_hi v138, v2 offset:57344
	v_bfe_u32 v2, v11, 16, 1
	v_add3_u32 v2, v11, v2, s80
	ds_write_b16_d16_hi v138, v2 offset:57856
	v_bfe_u32 v2, v12, 16, 1
	v_add3_u32 v2, v12, v2, s80
	ds_write_b16_d16_hi v138, v2 offset:58368
	v_bfe_u32 v2, v13, 16, 1
	v_add3_u32 v2, v13, v2, s80
	ds_write_b16_d16_hi v138, v2 offset:58880
	v_bfe_u32 v2, v14, 16, 1
	v_add3_u32 v2, v14, v2, s80
	ds_write_b16_d16_hi v138, v2 offset:61440
	v_bfe_u32 v2, v15, 16, 1
	v_add3_u32 v2, v15, v2, s80
	ds_write_b16_d16_hi v138, v2 offset:61952
	v_bfe_u32 v2, v16, 16, 1
	v_add3_u32 v2, v16, v2, s80
	ds_write_b16_d16_hi v138, v2 offset:62464
	v_bfe_u32 v2, v17, 16, 1
	v_add3_u32 v2, v17, v2, s80
	ds_write_b16_d16_hi v138, v2 offset:62976
	v_lshl_add_u64 v[6:7], v[106:107], 0, s[0:1]
	global_load_dwordx4 v[2:5], v[6:7], off offset:16
	s_nop 0
	global_load_dwordx4 v[6:9], v[6:7], off
	s_waitcnt lgkmcnt(0)
	s_barrier
; #define GAS __attribute__((address_space(1)))
; #define LAS __attribute__((address_space(3)))
; __device__ __forceinline__ void sgu_unit(Frame& F, int unit) {
;     ...
; #pragma unroll
;     for (int i = 0; i < 8; ++i) { const v4u fw = *(const LAS v4u*)(L + (rs_ + 16 * i) * 512 + q_ * 16); const float bb = F.sgb[g * GMC + rs_ + 16 * i]; v2u o;
;         o.x = pk4_fp8(S_YB * bflo(uu[i].x) * (bflo(fw.x) * g0.x + bb), S_YB * bfhi(uu[i].x) * (bfhi(fw.x) * g0.y + bb), S_YB * bflo(uu[i].y) * (bflo(fw.y) * g0.z + bb), S_YB * bfhi(uu[i].y) * (bfhi(fw.y) * g0.w + bb));
;         o.y = pk4_fp8(S_YB * bflo(uu[i].z) * (bflo(fw.z) * g1.x + bb), S_YB * bfhi(uu[i].z) * (bfhi(fw.z) * g1.y + bb), S_YB * bflo(uu[i].w) * (bflo(fw.w) * g1.z + bb), S_YB * bfhi(uu[i].w) * (bfhi(fw.w) * g1.w + bb));
;         *(GAS v2u*)((unsigned char*)F.YA + (size_t)(r0 + rs_ + 16 * i) * (2 * ATTW) + ATTW + c0 + 8 * q_) = o; }
	v_lshlrev_b32_e32 v20, 2, v113
	global_load_dword v240, v20, s[8:9]
	global_load_dword v241, v20, s[8:9] offset:64
	global_load_dword v242, v20, s[8:9] offset:128
	global_load_dword v243, v20, s[8:9] offset:192
	global_load_dword v244, v20, s[8:9] offset:256
	global_load_dword v245, v20, s[8:9] offset:320
	global_load_dword v246, v20, s[8:9] offset:384
	global_load_dword v247, v20, s[8:9] offset:448
	ds_read_b128 v[10:13], v139
	s_waitcnt vmcnt(17)
	v_lshlrev_b32_e32 v14, 16, v94
	v_lshlrev_b32_e32 v16, 16, v95
	v_lshlrev_b32_e32 v22, 16, v97
	s_waitcnt lgkmcnt(0)
	v_lshlrev_b32_e32 v15, 16, v10
	v_lshlrev_b32_e32 v17, 16, v11
	v_and_b32_e32 v11, 0xffff0000, v11
	v_lshlrev_b32_e32 v23, 16, v13
	v_and_b32_e32 v13, 0xffff0000, v13
	s_waitcnt vmcnt(8)
	v_mov_b32_e32 v113, v6
	v_pk_mul_f32 v[14:15], v[112:113], v[14:15]
	s_waitcnt vmcnt(7)
	v_mov_b32_e32 v19, v240
	v_add_f32_e32 v6, v19, v15
	v_mul_f32_e32 v18, v14, v6
	v_and_b32_e32 v15, 0xffff0000, v10
	v_and_b32_e32 v14, 0xffff0000, v94
	v_mov_b32_e32 v6, v112
	v_pk_mul_f32 v[14:15], v[6:7], v[14:15]
	s_nop 0
	v_add_f32_e32 v10, v19, v15
	v_mul_f32_e32 v21, v14, v10
	v_mov_b32_e32 v14, v112
	v_mov_b32_e32 v15, v8
	v_pk_mul_f32 v[16:17], v[14:15], v[16:17]
	v_and_b32_e32 v10, 0xffff0000, v95
	v_add_f32_e32 v8, v19, v17
	v_mul_f32_e32 v16, v16, v8
	v_mov_b32_e32 v8, v112
	v_pk_mul_f32 v[10:11], v[8:9], v[10:11]
	v_med3_f32 v17, v21, s81, v149
	v_add_f32_e32 v11, v19, v11
	v_mul_f32_e32 v10, v10, v11
	v_med3_f32 v11, v18, s81, v149
	v_mov_b32_e32 v18, v101
	v_cvt_pk_fp8_f32 v18, v11, v17
	v_med3_f32 v11, v16, s81, v149
	v_med3_f32 v10, v10, s81, v149
	v_lshlrev_b32_e32 v16, 16, v96
	v_cvt_pk_fp8_f32 v18, v11, v10 op_sel:[0,0,1]
	v_lshlrev_b32_e32 v17, 16, v12
	v_mov_b32_e32 v10, v112
	v_mov_b32_e32 v11, v2
	v_pk_mul_f32 v[16:17], v[10:11], v[16:17]
	s_nop 0
	v_add_f32_e32 v2, v19, v17
	v_mul_f32_e32 v21, v16, v2
	v_and_b32_e32 v17, 0xffff0000, v12
	v_and_b32_e32 v16, 0xffff0000, v96
	v_mov_b32_e32 v2, v112
	v_pk_mul_f32 v[16:17], v[2:3], v[16:17]
	s_nop 0
	v_add_f32_e32 v12, v19, v17
	v_mul_f32_e32 v24, v16, v12
	v_mov_b32_e32 v16, v112
	v_mov_b32_e32 v17, v4
	v_pk_mul_f32 v[22:23], v[16:17], v[22:23]
	v_and_b32_e32 v12, 0xffff0000, v97
	v_add_f32_e32 v4, v19, v23
	v_mul_f32_e32 v22, v22, v4
	v_mov_b32_e32 v4, v112
	v_pk_mul_f32 v[12:13], v[4:5], v[12:13]
	s_nop 0
	v_add_f32_e32 v13, v19, v13
	v_mul_f32_e32 v12, v12, v13
	v_med3_f32 v13, v21, s81, v149
	v_med3_f32 v21, v24, s81, v149
	v_mov_b32_e32 v19, v101
	v_cvt_pk_fp8_f32 v19, v13, v21
	v_med3_f32 v13, v22, s81, v149
	v_med3_f32 v12, v12, s81, v149
	ds_read_b128 v[22:25], v140
	v_cvt_pk_fp8_f32 v19, v13, v12 op_sel:[0,0,1]
	v_lshlrev_b64 v[12:13], 12, v[128:129]
	v_lshl_add_u64 v[12:13], s[68:69], 0, v[12:13]
	v_lshl_add_u64 v[12:13], v[12:13], 0, s[72:73]
	v_lshl_add_u64 v[12:13], v[12:13], 0, v[98:99]
	global_store_dwordx2 v[12:13], v[18:19], off offset:2048
	v_lshlrev_b32_e32 v12, 16, v90
	s_waitcnt lgkmcnt(0)
	v_lshlrev_b32_e32 v13, 16, v22
	v_pk_mul_f32 v[12:13], v[112:113], v[12:13]
	s_waitcnt vmcnt(7)
	v_mov_b32_e32 v21, v241
	v_add_f32_e32 v13, v21, v13
	v_mul_f32_e32 v18, v12, v13
	v_and_b32_e32 v13, 0xffff0000, v22
	v_and_b32_e32 v12, 0xffff0000, v90
	v_pk_mul_f32 v[12:13], v[6:7], v[12:13]
	v_med3_f32 v18, v18, s81, v149
	v_add_f32_e32 v13, v21, v13
	v_mul_f32_e32 v19, v12, v13
	v_lshlrev_b32_e32 v12, 16, v91
	v_lshlrev_b32_e32 v13, 16, v23
	v_pk_mul_f32 v[12:13], v[14:15], v[12:13]
	v_med3_f32 v19, v19, s81, v149
	v_add_f32_e32 v13, v21, v13
	v_mul_f32_e32 v22, v12, v13
	v_and_b32_e32 v13, 0xffff0000, v23
	v_and_b32_e32 v12, 0xffff0000, v91
	v_pk_mul_f32 v[12:13], v[8:9], v[12:13]
	s_nop 0
	v_add_f32_e32 v13, v21, v13
	v_mul_f32_e32 v13, v12, v13
	v_mov_b32_e32 v12, v101
	v_cvt_pk_fp8_f32 v12, v18, v19
	v_med3_f32 v18, v22, s81, v149
	v_med3_f32 v13, v13, s81, v149
	v_lshlrev_b32_e32 v19, 16, v24
	v_cvt_pk_fp8_f32 v12, v18, v13 op_sel:[0,0,1]
	v_lshlrev_b32_e32 v18, 16, v92
	v_pk_mul_f32 v[18:19], v[10:11], v[18:19]
	s_nop 0
	v_add_f32_e32 v13, v21, v19
	v_mul_f32_e32 v13, v18, v13
	v_and_b32_e32 v19, 0xffff0000, v24
	v_and_b32_e32 v18, 0xffff0000, v92
	v_pk_mul_f32 v[18:19], v[2:3], v[18:19]
	s_nop 0
	v_add_f32_e32 v19, v21, v19
	v_mul_f32_e32 v22, v18, v19
	v_lshlrev_b32_e32 v18, 16, v93
	v_lshlrev_b32_e32 v19, 16, v25
	v_pk_mul_f32 v[18:19], v[16:17], v[18:19]
	s_nop 0
	v_add_f32_e32 v19, v21, v19
	v_mul_f32_e32 v23, v18, v19
	v_and_b32_e32 v19, 0xffff0000, v25
	v_and_b32_e32 v18, 0xffff0000, v93
	v_pk_mul_f32 v[18:19], v[4:5], v[18:19]
	s_nop 0
	v_add_f32_e32 v19, v21, v19
	v_mul_f32_e32 v18, v18, v19
	v_med3_f32 v19, v13, s81, v149
	v_med3_f32 v21, v22, s81, v149
	v_mov_b32_e32 v13, v101
	v_cvt_pk_fp8_f32 v13, v19, v21
	v_med3_f32 v19, v23, s81, v149
	v_med3_f32 v18, v18, s81, v149
	ds_read_b128 v[22:25], v141
	v_cvt_pk_fp8_f32 v13, v19, v18 op_sel:[0,0,1]
	v_lshlrev_b64 v[18:19], 12, v[126:127]
	v_lshl_add_u64 v[18:19], s[68:69], 0, v[18:19]
	v_lshl_add_u64 v[18:19], v[18:19], 0, s[72:73]
	v_lshl_add_u64 v[18:19], v[18:19], 0, v[98:99]
	global_store_dwordx2 v[18:19], v[12:13], off offset:2048
	v_lshlrev_b32_e32 v12, 16, v86
	s_waitcnt lgkmcnt(0)
	v_lshlrev_b32_e32 v13, 16, v22
	v_pk_mul_f32 v[12:13], v[112:113], v[12:13]
	s_waitcnt vmcnt(7)
; #define GAS __attribute__((address_space(1)))
; #define LAS __attribute__((address_space(3)))
; __device__ __forceinline__ void sgu_unit(Frame& F, int unit) {
;     ...
; #pragma unroll
;     for (int i = 0; i < 8; ++i) { const v4u fw = *(const LAS v4u*)(L + (rs_ + 16 * i) * 512 + q_ * 16); const float bb = F.sgb[g * GMC + rs_ + 16 * i]; v2u o;
;         o.x = pk4_fp8(S_YB * bflo(uu[i].x) * (bflo(fw.x) * g0.x + bb), S_YB * bfhi(uu[i].x) * (bfhi(fw.x) * g0.y + bb), S_YB * bflo(uu[i].y) * (bflo(fw.y) * g0.z + bb), S_YB * bfhi(uu[i].y) * (bfhi(fw.y) * g0.w + bb));
;         o.y = pk4_fp8(S_YB * bflo(uu[i].z) * (bflo(fw.z) * g1.x + bb), S_YB * bfhi(uu[i].z) * (bfhi(fw.z) * g1.y + bb), S_YB * bflo(uu[i].w) * (bflo(fw.w) * g1.z + bb), S_YB * bfhi(uu[i].w) * (bfhi(fw.w) * g1.w + bb));
;         *(GAS v2u*)((unsigned char*)F.YA + (size_t)(r0 + rs_ + 16 * i) * (2 * ATTW) + ATTW + c0 + 8 * q_) = o; }
	v_mov_b32_e32 v21, v242
	v_add_f32_e32 v13, v21, v13
	v_mul_f32_e32 v18, v12, v13
	v_and_b32_e32 v13, 0xffff0000, v22
	v_and_b32_e32 v12, 0xffff0000, v86
	v_pk_mul_f32 v[12:13], v[6:7], v[12:13]
	v_med3_f32 v18, v18, s81, v149
	v_add_f32_e32 v13, v21, v13
	v_mul_f32_e32 v19, v12, v13
	v_lshlrev_b32_e32 v12, 16, v87
	v_lshlrev_b32_e32 v13, 16, v23
	v_pk_mul_f32 v[12:13], v[14:15], v[12:13]
	v_med3_f32 v19, v19, s81, v149
	v_add_f32_e32 v13, v21, v13
	v_mul_f32_e32 v22, v12, v13
	v_and_b32_e32 v13, 0xffff0000, v23
	v_and_b32_e32 v12, 0xffff0000, v87
	v_pk_mul_f32 v[12:13], v[8:9], v[12:13]
	s_nop 0
	v_add_f32_e32 v13, v21, v13
	v_mul_f32_e32 v13, v12, v13
	v_mov_b32_e32 v12, v101
	v_cvt_pk_fp8_f32 v12, v18, v19
	v_med3_f32 v18, v22, s81, v149
	v_med3_f32 v13, v13, s81, v149
	v_lshlrev_b32_e32 v19, 16, v24
	v_cvt_pk_fp8_f32 v12, v18, v13 op_sel:[0,0,1]
	v_lshlrev_b32_e32 v18, 16, v88
	v_pk_mul_f32 v[18:19], v[10:11], v[18:19]
	s_nop 0
	v_add_f32_e32 v13, v21, v19
	v_mul_f32_e32 v13, v18, v13
	v_and_b32_e32 v19, 0xffff0000, v24
	v_and_b32_e32 v18, 0xffff0000, v88
	v_pk_mul_f32 v[18:19], v[2:3], v[18:19]
	s_nop 0
	v_add_f32_e32 v19, v21, v19
	v_mul_f32_e32 v22, v18, v19
	v_lshlrev_b32_e32 v18, 16, v89
	v_lshlrev_b32_e32 v19, 16, v25
	v_pk_mul_f32 v[18:19], v[16:17], v[18:19]
	s_nop 0
	v_add_f32_e32 v19, v21, v19
	v_mul_f32_e32 v23, v18, v19
	v_and_b32_e32 v19, 0xffff0000, v25
	v_and_b32_e32 v18, 0xffff0000, v89
	v_pk_mul_f32 v[18:19], v[4:5], v[18:19]
	s_nop 0
	v_add_f32_e32 v19, v21, v19
	v_mul_f32_e32 v18, v18, v19
	v_med3_f32 v19, v13, s81, v149
	v_med3_f32 v21, v22, s81, v149
	v_mov_b32_e32 v13, v101
	v_cvt_pk_fp8_f32 v13, v19, v21
	v_med3_f32 v19, v23, s81, v149
	v_med3_f32 v18, v18, s81, v149
	ds_read_b128 v[22:25], v142
	v_cvt_pk_fp8_f32 v13, v19, v18 op_sel:[0,0,1]
	v_lshlrev_b64 v[18:19], 12, v[124:125]
	v_lshl_add_u64 v[18:19], s[68:69], 0, v[18:19]
	v_lshl_add_u64 v[18:19], v[18:19], 0, s[72:73]
	v_lshl_add_u64 v[18:19], v[18:19], 0, v[98:99]
	global_store_dwordx2 v[18:19], v[12:13], off offset:2048
	v_lshlrev_b32_e32 v12, 16, v82
	s_waitcnt lgkmcnt(0)
	v_lshlrev_b32_e32 v13, 16, v22
	v_pk_mul_f32 v[12:13], v[112:113], v[12:13]
	s_waitcnt vmcnt(7)
	v_mov_b32_e32 v21, v243
	v_add_f32_e32 v13, v21, v13
	v_mul_f32_e32 v18, v12, v13
	v_and_b32_e32 v13, 0xffff0000, v22
	v_and_b32_e32 v12, 0xffff0000, v82
	v_pk_mul_f32 v[12:13], v[6:7], v[12:13]
	v_med3_f32 v18, v18, s81, v149
	v_add_f32_e32 v13, v21, v13
	v_mul_f32_e32 v19, v12, v13
	v_lshlrev_b32_e32 v12, 16, v83
	v_lshlrev_b32_e32 v13, 16, v23
	v_pk_mul_f32 v[12:13], v[14:15], v[12:13]
	v_med3_f32 v19, v19, s81, v149
	v_add_f32_e32 v13, v21, v13
	v_mul_f32_e32 v22, v12, v13
	v_and_b32_e32 v13, 0xffff0000, v23
	v_and_b32_e32 v12, 0xffff0000, v83
	v_pk_mul_f32 v[12:13], v[8:9], v[12:13]
	s_nop 0
	v_add_f32_e32 v13, v21, v13
	v_mul_f32_e32 v13, v12, v13
	v_mov_b32_e32 v12, v101
	v_cvt_pk_fp8_f32 v12, v18, v19
	v_med3_f32 v18, v22, s81, v149
	v_med3_f32 v13, v13, s81, v149
	v_lshlrev_b32_e32 v19, 16, v24
	v_cvt_pk_fp8_f32 v12, v18, v13 op_sel:[0,0,1]
	v_lshlrev_b32_e32 v18, 16, v84
	v_pk_mul_f32 v[18:19], v[10:11], v[18:19]
	s_nop 0
	v_add_f32_e32 v13, v21, v19
	v_mul_f32_e32 v13, v18, v13
	v_and_b32_e32 v19, 0xffff0000, v24
	v_and_b32_e32 v18, 0xffff0000, v84
	v_pk_mul_f32 v[18:19], v[2:3], v[18:19]
	s_nop 0
	v_add_f32_e32 v19, v21, v19
	v_mul_f32_e32 v22, v18, v19
	v_lshlrev_b32_e32 v18, 16, v85
	v_lshlrev_b32_e32 v19, 16, v25
	v_pk_mul_f32 v[18:19], v[16:17], v[18:19]
	s_nop 0
	v_add_f32_e32 v19, v21, v19
	v_mul_f32_e32 v23, v18, v19
	v_and_b32_e32 v19, 0xffff0000, v25
	v_and_b32_e32 v18, 0xffff0000, v85
	v_pk_mul_f32 v[18:19], v[4:5], v[18:19]
	s_nop 0
	v_add_f32_e32 v19, v21, v19
	v_mul_f32_e32 v18, v18, v19
	v_med3_f32 v19, v13, s81, v149
	v_med3_f32 v21, v22, s81, v149
	v_mov_b32_e32 v13, v101
	v_cvt_pk_fp8_f32 v13, v19, v21
	v_med3_f32 v19, v23, s81, v149
	v_med3_f32 v18, v18, s81, v149
	ds_read_b128 v[22:25], v143
	v_cvt_pk_fp8_f32 v13, v19, v18 op_sel:[0,0,1]
	v_lshlrev_b64 v[18:19], 12, v[122:123]
	v_lshl_add_u64 v[18:19], s[68:69], 0, v[18:19]
	v_lshl_add_u64 v[18:19], v[18:19], 0, s[72:73]
	v_lshl_add_u64 v[18:19], v[18:19], 0, v[98:99]
	global_store_dwordx2 v[18:19], v[12:13], off offset:2048
	v_lshlrev_b32_e32 v12, 16, v78
	s_waitcnt lgkmcnt(0)
	v_lshlrev_b32_e32 v13, 16, v22
	v_pk_mul_f32 v[12:13], v[112:113], v[12:13]
	s_waitcnt vmcnt(7)
	v_mov_b32_e32 v21, v244
	v_add_f32_e32 v13, v21, v13
	v_mul_f32_e32 v18, v12, v13
	v_and_b32_e32 v13, 0xffff0000, v22
	v_and_b32_e32 v12, 0xffff0000, v78
	v_pk_mul_f32 v[12:13], v[6:7], v[12:13]
	v_med3_f32 v18, v18, s81, v149
	v_add_f32_e32 v13, v21, v13
	v_mul_f32_e32 v19, v12, v13
	v_lshlrev_b32_e32 v12, 16, v79
	v_lshlrev_b32_e32 v13, 16, v23
	v_pk_mul_f32 v[12:13], v[14:15], v[12:13]
	v_med3_f32 v19, v19, s81, v149
	v_add_f32_e32 v13, v21, v13
	v_mul_f32_e32 v22, v12, v13
	v_and_b32_e32 v13, 0xffff0000, v23
	v_and_b32_e32 v12, 0xffff0000, v79
	v_pk_mul_f32 v[12:13], v[8:9], v[12:13]
	s_nop 0
	v_add_f32_e32 v13, v21, v13
	v_mul_f32_e32 v13, v12, v13
	v_mov_b32_e32 v12, v101
	v_cvt_pk_fp8_f32 v12, v18, v19
	v_med3_f32 v18, v22, s81, v149
	v_med3_f32 v13, v13, s81, v149
	v_lshlrev_b32_e32 v19, 16, v24
	v_cvt_pk_fp8_f32 v12, v18, v13 op_sel:[0,0,1]
	v_lshlrev_b32_e32 v18, 16, v80
	v_pk_mul_f32 v[18:19], v[10:11], v[18:19]
	s_nop 0
	v_add_f32_e32 v13, v21, v19
	v_mul_f32_e32 v13, v18, v13
	v_and_b32_e32 v19, 0xffff0000, v24
	v_and_b32_e32 v18, 0xffff0000, v80
	v_pk_mul_f32 v[18:19], v[2:3], v[18:19]
	s_nop 0
	v_add_f32_e32 v19, v21, v19
	v_mul_f32_e32 v22, v18, v19
	v_lshlrev_b32_e32 v18, 16, v81
	v_lshlrev_b32_e32 v19, 16, v25
	v_pk_mul_f32 v[18:19], v[16:17], v[18:19]
	s_nop 0
	v_add_f32_e32 v19, v21, v19
	v_mul_f32_e32 v23, v18, v19
	v_and_b32_e32 v19, 0xffff0000, v25
	v_and_b32_e32 v18, 0xffff0000, v81
	v_pk_mul_f32 v[18:19], v[4:5], v[18:19]
	s_nop 0
	v_add_f32_e32 v19, v21, v19
	v_mul_f32_e32 v18, v18, v19
	v_med3_f32 v19, v13, s81, v149
	v_med3_f32 v21, v22, s81, v149
	v_mov_b32_e32 v13, v101
	v_cvt_pk_fp8_f32 v13, v19, v21
	v_med3_f32 v19, v23, s81, v149
	v_med3_f32 v18, v18, s81, v149
	ds_read_b128 v[22:25], v144
	v_cvt_pk_fp8_f32 v13, v19, v18 op_sel:[0,0,1]
	v_lshlrev_b64 v[18:19], 12, v[120:121]
	v_lshl_add_u64 v[18:19], s[68:69], 0, v[18:19]
	v_lshl_add_u64 v[18:19], v[18:19], 0, s[72:73]
	v_lshl_add_u64 v[18:19], v[18:19], 0, v[98:99]
	global_store_dwordx2 v[18:19], v[12:13], off offset:2048
	v_lshlrev_b32_e32 v12, 16, v74
	s_waitcnt lgkmcnt(0)
; #define GAS __attribute__((address_space(1)))
; #define LAS __attribute__((address_space(3)))
; __device__ __forceinline__ void sgu_unit(Frame& F, int unit) {
;     ...
; #pragma unroll
;     for (int i = 0; i < 8; ++i) { const v4u fw = *(const LAS v4u*)(L + (rs_ + 16 * i) * 512 + q_ * 16); const float bb = F.sgb[g * GMC + rs_ + 16 * i]; v2u o;
;         o.x = pk4_fp8(S_YB * bflo(uu[i].x) * (bflo(fw.x) * g0.x + bb), S_YB * bfhi(uu[i].x) * (bfhi(fw.x) * g0.y + bb), S_YB * bflo(uu[i].y) * (bflo(fw.y) * g0.z + bb), S_YB * bfhi(uu[i].y) * (bfhi(fw.y) * g0.w + bb));
;         o.y = pk4_fp8(S_YB * bflo(uu[i].z) * (bflo(fw.z) * g1.x + bb), S_YB * bfhi(uu[i].z) * (bfhi(fw.z) * g1.y + bb), S_YB * bflo(uu[i].w) * (bflo(fw.w) * g1.z + bb), S_YB * bfhi(uu[i].w) * (bfhi(fw.w) * g1.w + bb));
;         *(GAS v2u*)((unsigned char*)F.YA + (size_t)(r0 + rs_ + 16 * i) * (2 * ATTW) + ATTW + c0 + 8 * q_) = o; }
	v_lshlrev_b32_e32 v13, 16, v22
	v_pk_mul_f32 v[12:13], v[112:113], v[12:13]
	s_waitcnt vmcnt(7)
	v_mov_b32_e32 v21, v245
	v_add_f32_e32 v13, v21, v13
	v_mul_f32_e32 v18, v12, v13
	v_and_b32_e32 v13, 0xffff0000, v22
	v_and_b32_e32 v12, 0xffff0000, v74
	v_pk_mul_f32 v[12:13], v[6:7], v[12:13]
	v_med3_f32 v18, v18, s81, v149
	v_add_f32_e32 v13, v21, v13
	v_mul_f32_e32 v19, v12, v13
	v_lshlrev_b32_e32 v12, 16, v75
	v_lshlrev_b32_e32 v13, 16, v23
	v_pk_mul_f32 v[12:13], v[14:15], v[12:13]
	v_med3_f32 v19, v19, s81, v149
	v_add_f32_e32 v13, v21, v13
	v_mul_f32_e32 v22, v12, v13
	v_and_b32_e32 v13, 0xffff0000, v23
	v_and_b32_e32 v12, 0xffff0000, v75
	v_pk_mul_f32 v[12:13], v[8:9], v[12:13]
	s_nop 0
	v_add_f32_e32 v13, v21, v13
	v_mul_f32_e32 v13, v12, v13
	v_mov_b32_e32 v12, v101
	v_cvt_pk_fp8_f32 v12, v18, v19
	v_med3_f32 v18, v22, s81, v149
	v_med3_f32 v13, v13, s81, v149
	v_lshlrev_b32_e32 v19, 16, v24
	v_cvt_pk_fp8_f32 v12, v18, v13 op_sel:[0,0,1]
	v_lshlrev_b32_e32 v18, 16, v76
	v_pk_mul_f32 v[18:19], v[10:11], v[18:19]
	s_nop 0
	v_add_f32_e32 v13, v21, v19
	v_mul_f32_e32 v13, v18, v13
	v_and_b32_e32 v19, 0xffff0000, v24
	v_and_b32_e32 v18, 0xffff0000, v76
	v_pk_mul_f32 v[18:19], v[2:3], v[18:19]
	s_nop 0
	v_add_f32_e32 v19, v21, v19
	v_mul_f32_e32 v22, v18, v19
	v_lshlrev_b32_e32 v18, 16, v77
	v_lshlrev_b32_e32 v19, 16, v25
	v_pk_mul_f32 v[18:19], v[16:17], v[18:19]
	s_nop 0
	v_add_f32_e32 v19, v21, v19
	v_mul_f32_e32 v23, v18, v19
	v_and_b32_e32 v19, 0xffff0000, v25
	v_and_b32_e32 v18, 0xffff0000, v77
	v_pk_mul_f32 v[18:19], v[4:5], v[18:19]
	s_nop 0
	v_add_f32_e32 v19, v21, v19
	v_mul_f32_e32 v18, v18, v19
	v_med3_f32 v19, v13, s81, v149
	v_med3_f32 v21, v22, s81, v149
	v_mov_b32_e32 v13, v101
	v_cvt_pk_fp8_f32 v13, v19, v21
	v_med3_f32 v19, v23, s81, v149
	v_med3_f32 v18, v18, s81, v149
	ds_read_b128 v[22:25], v145
	v_cvt_pk_fp8_f32 v13, v19, v18 op_sel:[0,0,1]
	v_lshlrev_b64 v[18:19], 12, v[118:119]
	v_lshl_add_u64 v[18:19], s[68:69], 0, v[18:19]
	v_lshl_add_u64 v[18:19], v[18:19], 0, s[72:73]
	v_lshl_add_u64 v[18:19], v[18:19], 0, v[98:99]
	global_store_dwordx2 v[18:19], v[12:13], off offset:2048
	v_lshlrev_b32_e32 v12, 16, v70
	s_waitcnt lgkmcnt(0)
	v_lshlrev_b32_e32 v13, 16, v22
	v_pk_mul_f32 v[12:13], v[112:113], v[12:13]
	s_waitcnt vmcnt(7)
	v_mov_b32_e32 v21, v246
	v_add_f32_e32 v13, v21, v13
	v_mul_f32_e32 v18, v12, v13
	v_and_b32_e32 v13, 0xffff0000, v22
	v_and_b32_e32 v12, 0xffff0000, v70
	v_pk_mul_f32 v[12:13], v[6:7], v[12:13]
	v_med3_f32 v18, v18, s81, v149
	v_add_f32_e32 v13, v21, v13
	v_mul_f32_e32 v19, v12, v13
	v_lshlrev_b32_e32 v12, 16, v71
	v_lshlrev_b32_e32 v13, 16, v23
	v_pk_mul_f32 v[12:13], v[14:15], v[12:13]
	v_med3_f32 v19, v19, s81, v149
	v_add_f32_e32 v13, v21, v13
	v_mul_f32_e32 v22, v12, v13
	v_and_b32_e32 v13, 0xffff0000, v23
	v_and_b32_e32 v12, 0xffff0000, v71
	v_pk_mul_f32 v[12:13], v[8:9], v[12:13]
	s_nop 0
	v_add_f32_e32 v13, v21, v13
	v_mul_f32_e32 v13, v12, v13
	v_mov_b32_e32 v12, v101
	v_cvt_pk_fp8_f32 v12, v18, v19
	v_med3_f32 v18, v22, s81, v149
	v_med3_f32 v13, v13, s81, v149
	v_lshlrev_b32_e32 v19, 16, v24
	v_cvt_pk_fp8_f32 v12, v18, v13 op_sel:[0,0,1]
	v_lshlrev_b32_e32 v18, 16, v72
	v_pk_mul_f32 v[18:19], v[10:11], v[18:19]
	s_nop 0
	v_add_f32_e32 v13, v21, v19
	v_mul_f32_e32 v13, v18, v13
	v_and_b32_e32 v19, 0xffff0000, v24
	v_and_b32_e32 v18, 0xffff0000, v72
	v_pk_mul_f32 v[18:19], v[2:3], v[18:19]
	s_nop 0
	v_add_f32_e32 v19, v21, v19
	v_mul_f32_e32 v22, v18, v19
	v_lshlrev_b32_e32 v18, 16, v73
	v_lshlrev_b32_e32 v19, 16, v25
	v_pk_mul_f32 v[18:19], v[16:17], v[18:19]
	s_nop 0
	v_add_f32_e32 v19, v21, v19
	v_mul_f32_e32 v23, v18, v19
	v_and_b32_e32 v19, 0xffff0000, v25
	v_and_b32_e32 v18, 0xffff0000, v73
	v_pk_mul_f32 v[18:19], v[4:5], v[18:19]
	s_nop 0
	v_add_f32_e32 v19, v21, v19
	v_mul_f32_e32 v18, v18, v19
	v_med3_f32 v19, v13, s81, v149
	v_med3_f32 v21, v22, s81, v149
	v_mov_b32_e32 v13, v101
	v_cvt_pk_fp8_f32 v13, v19, v21
	v_med3_f32 v19, v23, s81, v149
	v_med3_f32 v18, v18, s81, v149
	ds_read_b128 v[22:25], v146
	v_cvt_pk_fp8_f32 v13, v19, v18 op_sel:[0,0,1]
	v_lshlrev_b64 v[18:19], 12, v[116:117]
	v_lshl_add_u64 v[18:19], s[68:69], 0, v[18:19]
	v_lshl_add_u64 v[18:19], v[18:19], 0, s[72:73]
	v_lshl_add_u64 v[18:19], v[18:19], 0, v[98:99]
	global_store_dwordx2 v[18:19], v[12:13], off offset:2048
	v_lshlrev_b32_e32 v12, 16, v66
	s_waitcnt lgkmcnt(0)
	v_lshlrev_b32_e32 v13, 16, v22
	v_pk_mul_f32 v[12:13], v[112:113], v[12:13]
	s_waitcnt vmcnt(7)
	v_mov_b32_e32 v18, v247
	v_add_f32_e32 v13, v18, v13
	v_mul_f32_e32 v19, v12, v13
	v_and_b32_e32 v13, 0xffff0000, v22
	v_and_b32_e32 v12, 0xffff0000, v66
	v_pk_mul_f32 v[6:7], v[6:7], v[12:13]
	s_nop 0
	v_add_f32_e32 v7, v18, v7
	v_mul_f32_e32 v12, v6, v7
	v_lshlrev_b32_e32 v6, 16, v67
	v_lshlrev_b32_e32 v7, 16, v23
	v_pk_mul_f32 v[6:7], v[14:15], v[6:7]
	s_nop 0
	v_add_f32_e32 v7, v18, v7
	v_mul_f32_e32 v13, v6, v7
	v_and_b32_e32 v7, 0xffff0000, v23
	v_and_b32_e32 v6, 0xffff0000, v67
	v_pk_mul_f32 v[6:7], v[8:9], v[6:7]
	v_med3_f32 v8, v19, s81, v149
	v_add_f32_e32 v7, v18, v7
	v_mul_f32_e32 v7, v6, v7
	v_med3_f32 v9, v12, s81, v149
	v_mov_b32_e32 v6, v101
	v_cvt_pk_fp8_f32 v6, v8, v9
	v_med3_f32 v8, v13, s81, v149
	v_med3_f32 v7, v7, s81, v149
	v_lshlrev_b32_e32 v9, 16, v24
	v_cvt_pk_fp8_f32 v6, v8, v7 op_sel:[0,0,1]
	v_lshlrev_b32_e32 v8, 16, v68
	v_pk_mul_f32 v[8:9], v[10:11], v[8:9]
	s_nop 0
	v_add_f32_e32 v7, v18, v9
	v_mul_f32_e32 v7, v8, v7
	v_and_b32_e32 v9, 0xffff0000, v24
	v_and_b32_e32 v8, 0xffff0000, v68
	v_pk_mul_f32 v[2:3], v[2:3], v[8:9]
	s_nop 0
	v_add_f32_e32 v3, v18, v3
	v_mul_f32_e32 v8, v2, v3
	v_lshlrev_b32_e32 v2, 16, v69
	v_lshlrev_b32_e32 v3, 16, v25
	v_pk_mul_f32 v[2:3], v[16:17], v[2:3]
	s_nop 0
	v_add_f32_e32 v3, v18, v3
	v_mul_f32_e32 v9, v2, v3
	v_and_b32_e32 v3, 0xffff0000, v25
	v_and_b32_e32 v2, 0xffff0000, v69
	v_pk_mul_f32 v[2:3], v[4:5], v[2:3]
	v_med3_f32 v4, v8, s81, v149
	v_add_f32_e32 v3, v18, v3
	v_mul_f32_e32 v2, v2, v3
	v_med3_f32 v3, v7, s81, v149
	v_mov_b32_e32 v7, v101
	v_cvt_pk_fp8_f32 v7, v3, v4
	v_med3_f32 v3, v9, s81, v149
	v_med3_f32 v2, v2, s81, v149
	v_cvt_pk_fp8_f32 v7, v3, v2 op_sel:[0,0,1]
	v_lshlrev_b64 v[2:3], 12, v[114:115]
	v_lshl_add_u64 v[2:3], s[68:69], 0, v[2:3]
	v_lshl_add_u64 v[2:3], v[2:3], 0, s[72:73]
	v_lshl_add_u64 v[2:3], v[2:3], 0, v[98:99]
	global_store_dwordx2 v[2:3], v[6:7], off offset:2048
	s_cbranch_scc0 .LBB0_1330
